# grid barrier exit: this CU's L1 invalidate (acquire) is issued on arrival and overlaps the wait for the other workgroups (only L1-bypassing polls/atomics run in between); the unused per-XCD relay add
# speedup vs baseline: 1.0186x; 1.0186x over previous
.LBB0_69:
	s_or_b64 exec, exec, s[10:11]
	v_cvt_f32_u32_e32 v5, v3
	s_waitcnt vmcnt(0)
	v_readfirstlane_b32 s8, v4
	v_sub_u32_e32 v4, 0, v3
	v_rcp_iflag_f32_e32 v5, v5
	v_add_u32_e32 v6, s8, v2
	v_mul_f32_e32 v5, 0x4f7ffffe, v5
	v_cvt_u32_f32_e32 v5, v5
	v_mul_lo_u32 v2, v4, v5
	v_mul_hi_u32 v2, v5, v2
	v_add_u32_e32 v2, v5, v2
	v_mul_hi_u32 v2, v6, v2
	v_mul_lo_u32 v4, v2, v3
	v_sub_u32_e32 v4, v6, v4
	v_add_u32_e32 v5, 1, v2
	v_cmp_ge_u32_e32 vcc, v4, v3
	s_nop 1
	v_cndmask_b32_e32 v2, v2, v5, vcc
	v_sub_u32_e32 v5, v4, v3
	v_cndmask_b32_e32 v4, v4, v5, vcc
	v_add_u32_e32 v5, 1, v2
	v_cmp_ge_u32_e32 vcc, v4, v3
	v_add_u32_e32 v4, 1, v6
	s_nop 0
	v_cndmask_b32_e32 v2, v2, v5, vcc
	v_mul_lo_u32 v5, v3, v2
	v_add_u32_e32 v3, v5, v3
	v_cmp_ne_u32_e32 vcc, v4, v3
	s_and_saveexec_b64 s[8:9], vcc
	s_xor_b64 s[8:9], exec, s[8:9]
	s_cbranch_execz .LBB0_83
	s_waitcnt lgkmcnt(0)
	buffer_inv sc1
	v_mov_b32_e32 v1, 0xb100
	global_load_dword v1, v1, s[40:41] offset:1024 sc1
	s_add_u32 s22, s40, 0xb500
	s_addc_u32 s23, s41, 0
	s_waitcnt vmcnt(0)
	v_cmp_eq_u32_e32 vcc, v1, v2
	s_and_saveexec_b64 s[10:11], vcc
	s_cbranch_execz .LBB0_82
	s_add_u32 s20, s40, 0x8200
	s_addc_u32 s21, s41, 0
	s_mov_b32 s38, 1
	s_mov_b64 s[24:25], 0
	v_mov_b32_e32 v1, 0
	s_branch .LBB0_73

.LBB0_82:
	s_or_b64 exec, exec, s[10:11]
	s_waitcnt vmcnt(0)
	s_waitcnt vmcnt(0)
.LBB0_83:
	s_andn2_saveexec_b64 s[8:9], s[8:9]
	s_cbranch_execz .LBB0_103
	s_mov_b64 s[8:9], exec
	buffer_wbl2 sc1
	buffer_inv sc1
	s_waitcnt lgkmcnt(0)
	s_waitcnt vmcnt(0)
	v_mbcnt_lo_u32_b32 v2, s8, 0
	v_mbcnt_hi_u32_b32 v2, s9, v2
	v_cmp_eq_u32_e32 vcc, 0, v2
	s_and_saveexec_b64 s[10:11], vcc
	s_cbranch_execz .LBB0_86
	s_bcnt1_i32_b64 s8, s[8:9]
	v_mov_b32_e32 v3, 0xb000
	v_mov_b32_e32 v4, s8
	global_atomic_add v3, v3, v4, s[40:41] offset:1024 sc0

.LBB0_100:
	s_or_b64 exec, exec, s[8:9]
	s_mov_b64 s[8:9], exec
	v_mbcnt_lo_u32_b32 v1, s8, 0
	v_mbcnt_hi_u32_b32 v1, s9, v1
	v_cmp_eq_u32_e32 vcc, 0, v1
	s_waitcnt vmcnt(0)
	s_and_saveexec_b64 s[10:11], vcc
	s_cbranch_execz .LBB0_102
	s_bcnt1_i32_b64 s8, s[8:9]
	v_mov_b32_e32 v1, 0x2000
	v_mov_b32_e32 v2, s8

.LBB0_267:
	s_or_b64 exec, exec, s[10:11]
	v_cvt_f32_u32_e32 v5, v3
	s_waitcnt vmcnt(0)
	v_readfirstlane_b32 s8, v4
	v_sub_u32_e32 v4, 0, v3
	v_rcp_iflag_f32_e32 v5, v5
	v_add_u32_e32 v6, s8, v2
	v_mul_f32_e32 v5, 0x4f7ffffe, v5
	v_cvt_u32_f32_e32 v5, v5
	v_mul_lo_u32 v2, v4, v5
	v_mul_hi_u32 v2, v5, v2
	v_add_u32_e32 v2, v5, v2
	v_mul_hi_u32 v2, v6, v2
	v_mul_lo_u32 v4, v2, v3
	v_sub_u32_e32 v4, v6, v4
	v_add_u32_e32 v5, 1, v2
	v_cmp_ge_u32_e32 vcc, v4, v3
	s_nop 1
	v_cndmask_b32_e32 v2, v2, v5, vcc
	v_sub_u32_e32 v5, v4, v3
	v_cndmask_b32_e32 v4, v4, v5, vcc
	v_add_u32_e32 v5, 1, v2
	v_cmp_ge_u32_e32 vcc, v4, v3
	v_add_u32_e32 v4, 1, v6
	s_nop 0
	v_cndmask_b32_e32 v2, v2, v5, vcc
	v_mul_lo_u32 v5, v3, v2
	v_add_u32_e32 v3, v5, v3
	v_cmp_ne_u32_e32 vcc, v4, v3
	s_and_saveexec_b64 s[8:9], vcc
	s_xor_b64 s[8:9], exec, s[8:9]
	s_cbranch_execz .LBB0_281
	s_waitcnt lgkmcnt(0)
	buffer_inv sc1
	v_mov_b32_e32 v1, 0xb100
	global_load_dword v1, v1, s[40:41] offset:1024 sc1
	s_add_u32 s14, s40, 0xb500
	s_addc_u32 s15, s41, 0
	s_waitcnt vmcnt(0)
	v_cmp_eq_u32_e32 vcc, v1, v2
	s_and_saveexec_b64 s[10:11], vcc
	s_cbranch_execz .LBB0_280
	s_add_u32 s12, s40, 0x8200
	s_addc_u32 s13, s41, 0
	s_mov_b32 s26, 1
	s_mov_b64 s[16:17], 0
	v_mov_b32_e32 v1, 0
	s_branch .LBB0_271

.LBB0_3506:
	s_or_b64 exec, exec, s[10:11]
	v_cvt_f32_u32_e32 v5, v3
	s_waitcnt vmcnt(0)
	v_readfirstlane_b32 s3, v4
	v_sub_u32_e32 v4, 0, v3
	v_rcp_iflag_f32_e32 v5, v5
	v_add_u32_e32 v6, s3, v2
	v_mul_f32_e32 v5, 0x4f7ffffe, v5
	v_cvt_u32_f32_e32 v5, v5
	v_mul_lo_u32 v2, v4, v5
	v_mul_hi_u32 v2, v5, v2
	v_add_u32_e32 v2, v5, v2
	v_mul_hi_u32 v2, v6, v2
	v_mul_lo_u32 v4, v2, v3
	v_sub_u32_e32 v4, v6, v4
	v_add_u32_e32 v5, 1, v2
	v_cmp_ge_u32_e32 vcc, v4, v3
	s_nop 1
	v_cndmask_b32_e32 v2, v2, v5, vcc
	v_sub_u32_e32 v5, v4, v3
	v_cndmask_b32_e32 v4, v4, v5, vcc
	v_add_u32_e32 v5, 1, v2
	v_cmp_ge_u32_e32 vcc, v4, v3
	v_add_u32_e32 v4, 1, v6
	s_nop 0
	v_cndmask_b32_e32 v2, v2, v5, vcc
	v_mul_lo_u32 v5, v3, v2
	v_add_u32_e32 v3, v5, v3
	v_cmp_ne_u32_e32 vcc, v4, v3
	s_and_saveexec_b64 s[8:9], vcc
	s_xor_b64 s[8:9], exec, s[8:9]
	s_cbranch_execz .LBB0_3520
	s_waitcnt lgkmcnt(0)
	buffer_inv sc1
	v_mov_b32_e32 v1, 0xb100
	global_load_dword v1, v1, s[40:41] offset:1024 sc1
	s_add_u32 s14, s40, 0xb500
	s_addc_u32 s15, s41, 0
	s_waitcnt vmcnt(0)
	v_cmp_eq_u32_e32 vcc, v1, v2
	s_and_saveexec_b64 s[10:11], vcc
	s_cbranch_execz .LBB0_3519
	s_add_u32 s12, s40, 0x8200
	s_addc_u32 s13, s41, 0
	s_mov_b32 s3, 1
	s_mov_b64 s[16:17], 0
	v_mov_b32_e32 v1, 0
	s_branch .LBB0_3510

.LBB0_3520:
	s_andn2_saveexec_b64 s[8:9], s[8:9]
	s_cbranch_execz .LBB0_3540
	s_mov_b64 s[8:9], exec
	buffer_wbl2 sc1
	buffer_inv sc1
	s_waitcnt lgkmcnt(0)
	s_waitcnt vmcnt(0)
	v_mbcnt_lo_u32_b32 v2, s8, 0
	v_mbcnt_hi_u32_b32 v2, s9, v2
	v_cmp_eq_u32_e32 vcc, 0, v2
	s_and_saveexec_b64 s[10:11], vcc
	s_cbranch_execz .LBB0_3523
	s_bcnt1_i32_b64 s3, s[8:9]
	v_mov_b32_e32 v3, 0xb000
	v_mov_b32_e32 v4, s3
	global_atomic_add v3, v3, v4, s[40:41] offset:1024 sc0

.LBB0_3537:
	s_or_b64 exec, exec, s[8:9]
	s_mov_b64 s[8:9], exec
	v_mbcnt_lo_u32_b32 v1, s8, 0
	v_mbcnt_hi_u32_b32 v1, s9, v1
	v_cmp_eq_u32_e32 vcc, 0, v1
	s_waitcnt vmcnt(0)
	s_and_saveexec_b64 s[10:11], vcc
	s_cbranch_execz .LBB0_3539
	s_bcnt1_i32_b64 s3, s[8:9]
	v_mov_b32_e32 v1, 0x2000
	v_mov_b32_e32 v2, s3
